# GLA inter-chunk scan (phase 4): its read-once loads and write-once stores marked nt
# speedup vs baseline: 1.0051x; 1.0051x over previous
.LBB0_807:
	v_or_b32_e32 v2, s4, v11
	v_lshlrev_b32_e32 v108, 2, v2
	v_or_b32_e32 v2, v108, v10
	v_lshlrev_b64 v[44:45], 13, v[2:3]
	v_lshl_or_b32 v2, v2, 5, v9
	v_lshl_add_u64 v[44:45], v[6:7], 0, v[44:45]
	v_lshl_add_u64 v[46:47], v[2:3], 2, s[18:19]
	v_or_b32_e32 v2, v108, v12
	global_load_dword v110, v[44:45], off nt
	global_load_dword v111, v[46:47], off nt
	v_lshlrev_b64 v[46:47], 13, v[2:3]
	v_lshl_or_b32 v2, v2, 5, v9
	v_lshl_add_u64 v[46:47], v[6:7], 0, v[46:47]
	v_lshl_add_u64 v[48:49], v[2:3], 2, s[18:19]
	v_or_b32_e32 v2, v108, v13
	global_load_dword v112, v[46:47], off nt
	global_load_dword v113, v[48:49], off nt
	v_lshlrev_b64 v[48:49], 13, v[2:3]
	v_lshl_or_b32 v2, v2, 5, v9
	v_lshl_add_u64 v[48:49], v[6:7], 0, v[48:49]
	v_lshl_add_u64 v[50:51], v[2:3], 2, s[18:19]
	v_or_b32_e32 v2, v108, v14
	global_load_dword v114, v[48:49], off nt
	global_load_dword v115, v[50:51], off nt
	v_lshlrev_b64 v[50:51], 13, v[2:3]
	v_lshl_or_b32 v2, v2, 5, v9
	v_lshl_add_u64 v[50:51], v[6:7], 0, v[50:51]
	v_lshl_add_u64 v[52:53], v[2:3], 2, s[18:19]
	v_or_b32_e32 v2, v108, v15
	global_load_dword v116, v[50:51], off nt
	global_load_dword v117, v[52:53], off nt
	v_lshlrev_b64 v[52:53], 13, v[2:3]
	v_lshl_or_b32 v2, v2, 5, v9
	v_lshl_add_u64 v[52:53], v[6:7], 0, v[52:53]
	v_lshl_add_u64 v[54:55], v[2:3], 2, s[18:19]
	v_or_b32_e32 v2, v108, v16
	global_load_dword v118, v[52:53], off nt
	global_load_dword v119, v[54:55], off nt
	v_lshlrev_b64 v[54:55], 13, v[2:3]
	v_lshl_or_b32 v2, v2, 5, v9
	v_lshl_add_u64 v[54:55], v[6:7], 0, v[54:55]
	v_lshl_add_u64 v[56:57], v[2:3], 2, s[18:19]
	v_or_b32_e32 v2, v108, v17
	global_load_dword v120, v[54:55], off nt
	global_load_dword v121, v[56:57], off nt
	v_lshlrev_b64 v[56:57], 13, v[2:3]
	v_lshl_or_b32 v2, v2, 5, v9
	v_lshl_add_u64 v[56:57], v[6:7], 0, v[56:57]
	v_lshl_add_u64 v[58:59], v[2:3], 2, s[18:19]
	v_or_b32_e32 v2, v108, v18
	global_load_dword v122, v[56:57], off nt
	global_load_dword v123, v[58:59], off nt
	v_lshlrev_b64 v[58:59], 13, v[2:3]
	v_lshl_or_b32 v2, v2, 5, v9
	v_lshl_add_u64 v[58:59], v[6:7], 0, v[58:59]
	v_lshl_add_u64 v[60:61], v[2:3], 2, s[18:19]
	v_or_b32_e32 v2, v108, v19
	global_load_dword v124, v[58:59], off nt
	global_load_dword v125, v[60:61], off nt
	v_lshlrev_b64 v[60:61], 13, v[2:3]
	v_lshl_or_b32 v2, v2, 5, v9
	v_lshl_add_u64 v[60:61], v[6:7], 0, v[60:61]
	v_lshl_add_u64 v[62:63], v[2:3], 2, s[18:19]
	v_or_b32_e32 v2, v108, v20
	global_load_dword v126, v[60:61], off nt
	global_load_dword v127, v[62:63], off nt
	v_lshlrev_b64 v[62:63], 13, v[2:3]
	v_lshl_or_b32 v2, v2, 5, v9
	v_lshl_add_u64 v[62:63], v[6:7], 0, v[62:63]
	v_lshl_add_u64 v[64:65], v[2:3], 2, s[18:19]
	v_or_b32_e32 v2, v108, v21
	global_load_dword v128, v[62:63], off nt
	global_load_dword v129, v[64:65], off nt
	v_lshlrev_b64 v[64:65], 13, v[2:3]
	v_lshl_or_b32 v2, v2, 5, v9
	v_lshl_add_u64 v[64:65], v[6:7], 0, v[64:65]
	v_lshl_add_u64 v[66:67], v[2:3], 2, s[18:19]
	v_or_b32_e32 v2, v108, v22
	global_load_dword v130, v[64:65], off nt
	global_load_dword v131, v[66:67], off nt
	v_lshlrev_b64 v[66:67], 13, v[2:3]
	v_lshl_or_b32 v2, v2, 5, v9
	v_lshl_add_u64 v[66:67], v[6:7], 0, v[66:67]
	v_lshl_add_u64 v[68:69], v[2:3], 2, s[18:19]
	v_or_b32_e32 v2, v108, v23
	global_load_dword v132, v[66:67], off nt
	global_load_dword v133, v[68:69], off nt
	v_lshlrev_b64 v[68:69], 13, v[2:3]
	v_lshl_or_b32 v2, v2, 5, v9
	v_lshl_add_u64 v[68:69], v[6:7], 0, v[68:69]
	v_lshl_add_u64 v[70:71], v[2:3], 2, s[18:19]
	v_or_b32_e32 v2, v108, v24
	global_load_dword v134, v[68:69], off nt
	global_load_dword v135, v[70:71], off nt
	v_lshlrev_b64 v[70:71], 13, v[2:3]
	v_lshl_or_b32 v2, v2, 5, v9
	v_lshl_add_u64 v[70:71], v[6:7], 0, v[70:71]
	v_lshl_add_u64 v[72:73], v[2:3], 2, s[18:19]
	v_or_b32_e32 v2, v108, v25
	global_load_dword v136, v[70:71], off nt
	global_load_dword v137, v[72:73], off nt
	v_lshlrev_b64 v[72:73], 13, v[2:3]
	v_lshl_or_b32 v2, v2, 5, v9
	v_lshl_add_u64 v[72:73], v[6:7], 0, v[72:73]
	v_lshl_add_u64 v[74:75], v[2:3], 2, s[18:19]
	v_or_b32_e32 v2, v108, v26
	global_load_dword v138, v[72:73], off nt
	global_load_dword v139, v[74:75], off nt
	v_lshlrev_b64 v[74:75], 13, v[2:3]
	v_lshl_or_b32 v2, v2, 5, v9
	v_lshl_add_u64 v[74:75], v[6:7], 0, v[74:75]
	v_lshl_add_u64 v[76:77], v[2:3], 2, s[18:19]
	v_or_b32_e32 v2, v108, v27
	global_load_dword v140, v[74:75], off nt
	global_load_dword v141, v[76:77], off nt
	v_lshlrev_b64 v[76:77], 13, v[2:3]
	v_lshl_or_b32 v2, v2, 5, v9
	v_lshl_add_u64 v[76:77], v[6:7], 0, v[76:77]
	v_lshl_add_u64 v[78:79], v[2:3], 2, s[18:19]
	v_or_b32_e32 v2, v108, v28
	global_load_dword v142, v[76:77], off nt
	global_load_dword v143, v[78:79], off nt
	v_lshlrev_b64 v[78:79], 13, v[2:3]
	v_lshl_or_b32 v2, v2, 5, v9
	v_lshl_add_u64 v[78:79], v[6:7], 0, v[78:79]
	v_lshl_add_u64 v[80:81], v[2:3], 2, s[18:19]
	v_or_b32_e32 v2, v108, v29
	global_load_dword v144, v[78:79], off nt
	global_load_dword v145, v[80:81], off nt
	v_lshlrev_b64 v[80:81], 13, v[2:3]
	v_lshl_or_b32 v2, v2, 5, v9
	v_lshl_add_u64 v[80:81], v[6:7], 0, v[80:81]
	v_lshl_add_u64 v[82:83], v[2:3], 2, s[18:19]
	v_or_b32_e32 v2, v108, v30
	global_load_dword v146, v[80:81], off nt
	global_load_dword v147, v[82:83], off nt
	v_lshlrev_b64 v[82:83], 13, v[2:3]
	v_lshl_or_b32 v2, v2, 5, v9
	v_lshl_add_u64 v[82:83], v[6:7], 0, v[82:83]
	v_lshl_add_u64 v[84:85], v[2:3], 2, s[18:19]
	v_or_b32_e32 v2, v108, v31
	global_load_dword v148, v[82:83], off nt
	global_load_dword v149, v[84:85], off nt
	v_lshlrev_b64 v[84:85], 13, v[2:3]
	v_lshl_or_b32 v2, v2, 5, v9
	v_lshl_add_u64 v[84:85], v[6:7], 0, v[84:85]
	v_lshl_add_u64 v[86:87], v[2:3], 2, s[18:19]
	v_or_b32_e32 v2, v108, v32
	global_load_dword v150, v[84:85], off nt
	global_load_dword v151, v[86:87], off nt
	v_lshlrev_b64 v[86:87], 13, v[2:3]
	v_lshl_or_b32 v2, v2, 5, v9
	v_lshl_add_u64 v[86:87], v[6:7], 0, v[86:87]
	v_lshl_add_u64 v[88:89], v[2:3], 2, s[18:19]
	v_or_b32_e32 v2, v108, v33
	global_load_dword v152, v[86:87], off nt
	global_load_dword v153, v[88:89], off nt
	v_lshlrev_b64 v[88:89], 13, v[2:3]
	v_lshl_or_b32 v2, v2, 5, v9
	v_lshl_add_u64 v[88:89], v[6:7], 0, v[88:89]
	v_lshl_add_u64 v[90:91], v[2:3], 2, s[18:19]
	v_or_b32_e32 v2, v108, v34
	global_load_dword v154, v[88:89], off nt
	global_load_dword v155, v[90:91], off nt
	v_lshlrev_b64 v[90:91], 13, v[2:3]
	v_lshl_or_b32 v2, v2, 5, v9
	v_lshl_add_u64 v[90:91], v[6:7], 0, v[90:91]
	v_lshl_add_u64 v[92:93], v[2:3], 2, s[18:19]
	v_or_b32_e32 v2, v108, v35
	global_load_dword v156, v[90:91], off nt
	global_load_dword v157, v[92:93], off nt
	v_lshlrev_b64 v[92:93], 13, v[2:3]
	v_lshl_or_b32 v2, v2, 5, v9
	v_lshl_add_u64 v[92:93], v[6:7], 0, v[92:93]
	v_lshl_add_u64 v[94:95], v[2:3], 2, s[18:19]
	v_or_b32_e32 v2, v108, v36
	global_load_dword v158, v[92:93], off nt
	global_load_dword v159, v[94:95], off nt
	v_lshlrev_b64 v[94:95], 13, v[2:3]
	v_lshl_or_b32 v2, v2, 5, v9
	v_lshl_add_u64 v[94:95], v[6:7], 0, v[94:95]
	v_lshl_add_u64 v[96:97], v[2:3], 2, s[18:19]
	v_or_b32_e32 v2, v108, v37
	global_load_dword v160, v[94:95], off nt
	global_load_dword v161, v[96:97], off nt
	v_lshlrev_b64 v[96:97], 13, v[2:3]
	v_lshl_or_b32 v2, v2, 5, v9
	v_lshl_add_u64 v[96:97], v[6:7], 0, v[96:97]
	v_lshl_add_u64 v[98:99], v[2:3], 2, s[18:19]
	v_or_b32_e32 v2, v108, v38
	global_load_dword v162, v[96:97], off nt
	global_load_dword v163, v[98:99], off nt
	v_lshlrev_b64 v[98:99], 13, v[2:3]
	v_lshl_or_b32 v2, v2, 5, v9
	v_lshl_add_u64 v[98:99], v[6:7], 0, v[98:99]
	v_lshl_add_u64 v[100:101], v[2:3], 2, s[18:19]
	v_or_b32_e32 v2, v108, v39
	global_load_dword v164, v[98:99], off nt
	global_load_dword v165, v[100:101], off nt
	v_lshlrev_b64 v[100:101], 13, v[2:3]
	v_lshl_or_b32 v2, v2, 5, v9
	v_lshl_add_u64 v[100:101], v[6:7], 0, v[100:101]
	v_lshl_add_u64 v[102:103], v[2:3], 2, s[18:19]
	v_or_b32_e32 v2, v108, v40
	global_load_dword v166, v[100:101], off nt
	global_load_dword v167, v[102:103], off nt
	v_lshlrev_b64 v[102:103], 13, v[2:3]
	v_lshl_or_b32 v2, v2, 5, v9
	v_lshl_add_u64 v[102:103], v[6:7], 0, v[102:103]
	v_lshl_add_u64 v[104:105], v[2:3], 2, s[18:19]
	v_or_b32_e32 v2, v108, v41
	global_load_dword v168, v[102:103], off nt
	global_load_dword v169, v[104:105], off nt
	v_lshlrev_b64 v[104:105], 13, v[2:3]
	v_lshl_or_b32 v2, v2, 5, v9
	v_lshl_add_u64 v[104:105], v[6:7], 0, v[104:105]
	v_lshl_add_u64 v[106:107], v[2:3], 2, s[18:19]
	v_or_b32_e32 v2, v108, v42
	global_load_dword v170, v[104:105], off nt
	global_load_dword v171, v[106:107], off nt
	v_lshlrev_b64 v[106:107], 13, v[2:3]
	v_lshl_or_b32 v2, v2, 5, v9
	v_lshl_add_u64 v[106:107], v[6:7], 0, v[106:107]
	v_lshl_add_u64 v[108:109], v[2:3], 2, s[18:19]
	global_load_dword v2, v[106:107], off nt
	s_nop 0
	global_load_dword v108, v[108:109], off nt
	s_mov_b32 s4, 32
	global_store_dword v[44:45], v43, off nt
	s_waitcnt vmcnt(0)
	v_add_f32_e32 v43, v43, v110
	v_fmac_f32_e32 v112, v111, v43
	v_mul_f32_e32 v44, v111, v43
	v_mul_f32_e32 v43, v113, v112
	v_fmac_f32_e32 v114, v113, v112
	global_store_dword v[48:49], v43, off nt
	v_mul_f32_e32 v43, v115, v114
	v_fmac_f32_e32 v116, v115, v114
	global_store_dword v[50:51], v43, off nt
	v_mul_f32_e32 v43, v117, v116
	v_fmac_f32_e32 v118, v117, v116
	global_store_dword v[52:53], v43, off nt
	v_mul_f32_e32 v43, v119, v118
	v_fmac_f32_e32 v120, v119, v118
	global_store_dword v[54:55], v43, off nt
	v_mul_f32_e32 v43, v121, v120
	v_fmac_f32_e32 v122, v121, v120
	global_store_dword v[56:57], v43, off nt
	v_mul_f32_e32 v43, v123, v122
	v_fmac_f32_e32 v124, v123, v122
	global_store_dword v[58:59], v43, off nt
	v_mul_f32_e32 v43, v125, v124
	v_fmac_f32_e32 v126, v125, v124
	global_store_dword v[60:61], v43, off nt
	v_mul_f32_e32 v43, v127, v126
	v_fmac_f32_e32 v128, v127, v126
	global_store_dword v[62:63], v43, off nt
	v_mul_f32_e32 v43, v129, v128
	v_fmac_f32_e32 v130, v129, v128
	global_store_dword v[64:65], v43, off nt
	v_mul_f32_e32 v43, v131, v130
	v_fmac_f32_e32 v132, v131, v130
	global_store_dword v[66:67], v43, off nt
	v_mul_f32_e32 v43, v133, v132
	v_fmac_f32_e32 v134, v133, v132
	global_store_dword v[68:69], v43, off nt
	v_mul_f32_e32 v43, v135, v134
	v_fmac_f32_e32 v136, v135, v134
	global_store_dword v[70:71], v43, off nt
	v_mul_f32_e32 v43, v137, v136
	v_fmac_f32_e32 v138, v137, v136
	global_store_dword v[72:73], v43, off nt
	v_mul_f32_e32 v43, v139, v138
	v_fmac_f32_e32 v140, v139, v138
	global_store_dword v[74:75], v43, off nt
	v_mul_f32_e32 v43, v141, v140
	v_fmac_f32_e32 v142, v141, v140
	global_store_dword v[76:77], v43, off nt
	v_mul_f32_e32 v43, v143, v142
	v_fmac_f32_e32 v144, v143, v142
	global_store_dword v[78:79], v43, off nt
	v_mul_f32_e32 v43, v145, v144
	v_fmac_f32_e32 v146, v145, v144
	global_store_dword v[80:81], v43, off nt
	v_mul_f32_e32 v43, v147, v146
	v_fmac_f32_e32 v148, v147, v146
	global_store_dword v[82:83], v43, off nt
	v_mul_f32_e32 v43, v149, v148
	v_fmac_f32_e32 v150, v149, v148
	global_store_dword v[84:85], v43, off nt
	v_mul_f32_e32 v43, v151, v150
	v_fmac_f32_e32 v152, v151, v150
	global_store_dword v[86:87], v43, off nt
	v_mul_f32_e32 v43, v153, v152
	v_fmac_f32_e32 v154, v153, v152
	global_store_dword v[88:89], v43, off nt
	v_mul_f32_e32 v43, v155, v154
	v_fmac_f32_e32 v156, v155, v154
	global_store_dword v[90:91], v43, off nt
	v_mul_f32_e32 v43, v157, v156
	v_fmac_f32_e32 v158, v157, v156
	global_store_dword v[92:93], v43, off nt
	v_mul_f32_e32 v43, v159, v158
	v_fmac_f32_e32 v160, v159, v158
	global_store_dword v[94:95], v43, off nt
	v_mul_f32_e32 v43, v161, v160
	v_fmac_f32_e32 v162, v161, v160
	global_store_dword v[96:97], v43, off nt
	v_mul_f32_e32 v43, v163, v162
	v_fmac_f32_e32 v164, v163, v162
	global_store_dword v[98:99], v43, off nt
	v_mul_f32_e32 v43, v165, v164
	v_fmac_f32_e32 v166, v165, v164
	global_store_dword v[100:101], v43, off nt
	v_mul_f32_e32 v43, v167, v166
	v_fmac_f32_e32 v168, v167, v166
	global_store_dword v[102:103], v43, off nt
	v_mul_f32_e32 v43, v169, v168
	v_fmac_f32_e32 v170, v169, v168
	global_store_dword v[104:105], v43, off nt
	v_mul_f32_e32 v43, v171, v170
	v_fmac_f32_e32 v2, v171, v170
	s_and_b64 vcc, exec, s[22:23]
	s_mov_b64 s[22:23], 0
	global_store_dword v[106:107], v43, off nt
	v_mul_f32_e32 v43, v108, v2
	global_store_dword v[46:47], v44, off nt
	s_cbranch_vccnz .LBB0_807
	s_branch .LBB0_804
